# speedup vs baseline: 1.0670x; 1.0670x over previous
_Z8dog_mainPKfS0_S0_S0_S0_S0_S0_Pf:
	s_load_dwordx8 s[12:19], s[0:1], 0x0
	s_load_dwordx8 s[20:27], s[0:1], 0x20
	s_and_b32 s3, s2, 7
	s_lshl_b32 s3, s3, 5
	s_lshr_b32 s4, s2, 3
	s_add_i32 s4, s3, s4
	s_and_b32 s6, s4, 3
	s_lshr_b32 s7, s4, 2
	s_mov_b32 s5, 0
	s_lshl_b64 s[8:9], s[4:5], 18
	v_and_b32_e32 v1, 63, v0
	v_lshrrev_b32_e32 v2, 6, v0
	v_and_b32_e32 v3, 15, v0
	v_and_b32_e32 v7, 31, v0
	v_lshl_or_b32 v4, v2, 5, v3
	v_lshl_or_b32 v5, v2, 5, v7
	v_lshlrev_b32_e32 v4, 2, v4
	v_lshlrev_b32_e32 v5, 2, v5
	v_lshlrev_b32_e32 v6, 4, v1
	v_lshl_or_b32 v6, v2, 12, v6
	v_bfe_u32 v7, v0, 4, 2
	s_waitcnt lgkmcnt(0)
	global_load_dword v32, v4, s[18:19]
	global_load_dword v33, v4, s[20:21]
	global_load_dword v34, v4, s[22:23]
	global_load_dword v35, v4, s[24:25]
	global_load_dword v36, v4, s[14:15]
	global_load_dword v37, v4, s[16:17]
	global_load_dword v38, v4, s[18:19] offset:64
	global_load_dword v39, v4, s[20:21] offset:64
	global_load_dword v40, v4, s[22:23] offset:64
	global_load_dword v41, v4, s[24:25] offset:64
	global_load_dword v42, v4, s[14:15] offset:64
	global_load_dword v43, v4, s[16:17] offset:64
	s_add_u32 s12, s12, s8
	s_addc_u32 s13, s13, s9
	global_load_dwordx4 v[128:131], v6, s[12:13] offset:0 nt
	global_load_dwordx4 v[132:135], v6, s[12:13] offset:1024 nt
	global_load_dwordx4 v[136:139], v6, s[12:13] offset:2048 nt
	global_load_dwordx4 v[140:143], v6, s[12:13] offset:3072 nt
	v_add_u32_e32 v6, 0x8000, v6
	global_load_dwordx4 v[144:147], v6, s[12:13] offset:0 nt
	global_load_dwordx4 v[148:151], v6, s[12:13] offset:1024 nt
	global_load_dwordx4 v[152:155], v6, s[12:13] offset:2048 nt
	global_load_dwordx4 v[156:159], v6, s[12:13] offset:3072 nt
	v_and_b32_e32 v16, 1, v0
	v_cmp_eq_u32_e64 s[30:31], 0, v16
	v_and_b32_e32 v17, 2, v0
	v_cmp_eq_u32_e64 s[32:33], 0, v17
	v_and_b32_e32 v16, 3, v0
	v_lshrrev_b32_e32 v17, 2, v1
	v_lshlrev_b32_e32 v16, 5, v16
	v_lshl_add_u32 v16, v17, 1, v16
	v_lshrrev_b32_e32 v17, 1, v2
	s_movk_i32 s10, 0x110
	v_mad_u32_u24 v16, v17, s10, v16
	v_and_b32_e32 v17, 1, v2
	v_lshl_add_u32 v14, v17, 7, v16
	v_lshlrev_b32_e32 v17, 4, v7
	v_mad_u32_u24 v15, v3, s10, v17
	s_lshl_b32 s11, s6, 5
	v_lshl_add_u32 v18, v7, 2, s11
	v_cvt_f32_u32_e32 v18, v18
	v_lshlrev_b32_e32 v19, 3, v7
	v_cvt_f32_u32_e32 v19, v19
	s_waitcnt vmcnt(8)
	v_add_f32_e32 v33, v32, v33
	v_sub_f32_e32 v12, v19, v34
	v_sub_f32_e32 v13, v18, v35
	v_rcp_f32_e32 v34, v32
	v_rcp_f32_e32 v35, v33
	s_nop 0
	v_fma_f32 v20, -v32, v34, 1.0
	v_fma_f32 v34, v20, v34, v34
	v_fma_f32 v20, -v33, v35, 1.0
	v_fma_f32 v35, v20, v35, v35
	v_mul_f32_e32 v8, 0xbf38aa3b, v34
	v_mul_f32_e32 v9, 0xbf38aa3b, v35
	v_mul_f32_e32 v36, v36, v34
	v_mul_f32_e32 v37, v37, v35
	v_mul_f32_e32 v10, 0x3e22f983, v36
	v_mul_f32_e32 v11, 0x3e22f983, v37
	v_add_f32_e32 v39, v38, v39
	v_sub_f32_e32 v2, v19, v40
	v_sub_f32_e32 v3, v18, v41
	v_rcp_f32_e32 v40, v38
	v_rcp_f32_e32 v41, v39
	s_nop 0
	v_fma_f32 v20, -v38, v40, 1.0
	v_fma_f32 v40, v20, v40, v40
	v_fma_f32 v20, -v39, v41, 1.0
	v_fma_f32 v41, v20, v41, v41
	v_mul_f32_e32 v28, 0xbf38aa3b, v40
	v_mul_f32_e32 v29, 0xbf38aa3b, v41
	v_mul_f32_e32 v42, v42, v40
	v_mul_f32_e32 v43, v43, v41
	v_mul_f32_e32 v30, 0x3e22f983, v42
	v_mul_f32_e32 v31, 0x3e22f983, v43
	s_getpc_b64 s[44:45]
.Lpc_anchor:
	s_add_u32 s44, s44, _Z7dog_finPKfS0_Pf-.Lpc_anchor
	s_addc_u32 s45, s45, 0
	s_load_dwordx16 s[48:63], s[44:45], 0x0
	s_load_dwordx16 s[64:79], s[44:45], 0x40
	s_load_dwordx16 s[80:95], s[44:45], 0x80
	v_mul_f32_e32 v16, v12, v12
	v_add_f32_e32 v17, 0x3f800000, v12
	v_add_f32_e32 v18, 0x40000000, v12
	v_add_f32_e32 v19, 0x40400000, v12
	v_mul_f32_e32 v17, v17, v17
	v_mul_f32_e32 v18, v18, v18
	v_mul_f32_e32 v19, v19, v19
	v_mul_f32_e32 v20, v8, v16
	v_mul_f32_e32 v24, v9, v16
	v_mul_f32_e32 v21, v8, v17
	v_mul_f32_e32 v25, v9, v17
	v_mul_f32_e32 v22, v8, v18
	v_mul_f32_e32 v26, v9, v18
	v_mul_f32_e32 v23, v8, v19
	v_mul_f32_e32 v27, v9, v19
	v_exp_f32_e32 v20, v20
	v_exp_f32_e32 v21, v21
	v_exp_f32_e32 v22, v22
	v_exp_f32_e32 v23, v23
	v_exp_f32_e32 v24, v24
	v_exp_f32_e32 v25, v25
	v_exp_f32_e32 v26, v26
	v_exp_f32_e32 v27, v27
	v_cvt_pk_f16_f32 v32, v20, v21
	v_cvt_pk_f16_f32 v33, v22, v23
	v_cvt_pk_f16_f32 v64, v24, v25
	v_cvt_pk_f16_f32 v65, v26, v27
	v_add_f32_e32 v16, 0x40800000, v12
	v_add_f32_e32 v17, 0x40a00000, v12
	v_add_f32_e32 v18, 0x40c00000, v12
	v_add_f32_e32 v19, 0x40e00000, v12
	v_mul_f32_e32 v16, v16, v16
	v_mul_f32_e32 v17, v17, v17
	v_mul_f32_e32 v18, v18, v18
	v_mul_f32_e32 v19, v19, v19
	v_mul_f32_e32 v20, v8, v16
	v_mul_f32_e32 v24, v9, v16
	v_mul_f32_e32 v21, v8, v17
	v_mul_f32_e32 v25, v9, v17
	v_mul_f32_e32 v22, v8, v18
	v_mul_f32_e32 v26, v9, v18
	v_mul_f32_e32 v23, v8, v19
	v_mul_f32_e32 v27, v9, v19
	v_exp_f32_e32 v20, v20
	v_exp_f32_e32 v21, v21
	v_exp_f32_e32 v22, v22
	v_exp_f32_e32 v23, v23
	v_exp_f32_e32 v24, v24
	v_exp_f32_e32 v25, v25
	v_exp_f32_e32 v26, v26
	v_exp_f32_e32 v27, v27
	v_cvt_pk_f16_f32 v34, v20, v21
	v_cvt_pk_f16_f32 v35, v22, v23
	v_cvt_pk_f16_f32 v66, v24, v25
	v_cvt_pk_f16_f32 v67, v26, v27
	v_add_f32_e32 v16, 0x42000000, v12
	v_add_f32_e32 v17, 0x42040000, v12
	v_add_f32_e32 v18, 0x42080000, v12
	v_add_f32_e32 v19, 0x420c0000, v12
	v_mul_f32_e32 v16, v16, v16
	v_mul_f32_e32 v17, v17, v17
	v_mul_f32_e32 v18, v18, v18
	v_mul_f32_e32 v19, v19, v19
	v_mul_f32_e32 v20, v8, v16
	v_mul_f32_e32 v24, v9, v16
	v_mul_f32_e32 v21, v8, v17
	v_mul_f32_e32 v25, v9, v17
	v_mul_f32_e32 v22, v8, v18
	v_mul_f32_e32 v26, v9, v18
	v_mul_f32_e32 v23, v8, v19
	v_mul_f32_e32 v27, v9, v19
	v_exp_f32_e32 v20, v20
	v_exp_f32_e32 v21, v21
	v_exp_f32_e32 v22, v22
	v_exp_f32_e32 v23, v23
	v_exp_f32_e32 v24, v24
	v_exp_f32_e32 v25, v25
	v_exp_f32_e32 v26, v26
	v_exp_f32_e32 v27, v27
	v_cvt_pk_f16_f32 v36, v20, v21
	v_cvt_pk_f16_f32 v37, v22, v23
	v_cvt_pk_f16_f32 v68, v24, v25
	v_cvt_pk_f16_f32 v69, v26, v27
	v_add_f32_e32 v16, 0x42100000, v12
	v_add_f32_e32 v17, 0x42140000, v12
	v_add_f32_e32 v18, 0x42180000, v12
	v_add_f32_e32 v19, 0x421c0000, v12
	v_mul_f32_e32 v16, v16, v16
	v_mul_f32_e32 v17, v17, v17
	v_mul_f32_e32 v18, v18, v18
	v_mul_f32_e32 v19, v19, v19
	v_mul_f32_e32 v20, v8, v16
	v_mul_f32_e32 v24, v9, v16
	v_mul_f32_e32 v21, v8, v17
	v_mul_f32_e32 v25, v9, v17
	v_mul_f32_e32 v22, v8, v18
	v_mul_f32_e32 v26, v9, v18
	v_mul_f32_e32 v23, v8, v19
	v_mul_f32_e32 v27, v9, v19
	v_exp_f32_e32 v20, v20
	v_exp_f32_e32 v21, v21
	v_exp_f32_e32 v22, v22
	v_exp_f32_e32 v23, v23
	v_exp_f32_e32 v24, v24
	v_exp_f32_e32 v25, v25
	v_exp_f32_e32 v26, v26
	v_exp_f32_e32 v27, v27
	v_cvt_pk_f16_f32 v38, v20, v21
	v_cvt_pk_f16_f32 v39, v22, v23
	v_cvt_pk_f16_f32 v70, v24, v25
	v_cvt_pk_f16_f32 v71, v26, v27
	v_add_u32_e32 v6, 0x8000, v6
	global_load_dwordx4 v[160:163], v6, s[12:13] offset:0 nt
	global_load_dwordx4 v[164:167], v6, s[12:13] offset:1024 nt
	global_load_dwordx4 v[168:171], v6, s[12:13] offset:2048 nt
	global_load_dwordx4 v[172:175], v6, s[12:13] offset:3072 nt
	v_add_f32_e32 v16, 0x42800000, v12
	v_add_f32_e32 v17, 0x42820000, v12
	v_add_f32_e32 v18, 0x42840000, v12
	v_add_f32_e32 v19, 0x42860000, v12
	v_mul_f32_e32 v16, v16, v16
	v_mul_f32_e32 v17, v17, v17
	v_mul_f32_e32 v18, v18, v18
	v_mul_f32_e32 v19, v19, v19
	v_mul_f32_e32 v20, v8, v16
	v_mul_f32_e32 v24, v9, v16
	v_mul_f32_e32 v21, v8, v17
	v_mul_f32_e32 v25, v9, v17
	v_mul_f32_e32 v22, v8, v18
	v_mul_f32_e32 v26, v9, v18
	v_mul_f32_e32 v23, v8, v19
	v_mul_f32_e32 v27, v9, v19
	v_exp_f32_e32 v20, v20
	v_exp_f32_e32 v21, v21
	v_exp_f32_e32 v22, v22
	v_exp_f32_e32 v23, v23
	v_exp_f32_e32 v24, v24
	v_exp_f32_e32 v25, v25
	v_exp_f32_e32 v26, v26
	v_exp_f32_e32 v27, v27
	v_cvt_pk_f16_f32 v40, v20, v21
	v_cvt_pk_f16_f32 v41, v22, v23
	v_cvt_pk_f16_f32 v72, v24, v25
	v_cvt_pk_f16_f32 v73, v26, v27
	v_add_f32_e32 v16, 0x42880000, v12
	v_add_f32_e32 v17, 0x428a0000, v12
	v_add_f32_e32 v18, 0x428c0000, v12
	v_add_f32_e32 v19, 0x428e0000, v12
	v_mul_f32_e32 v16, v16, v16
	v_mul_f32_e32 v17, v17, v17
	v_mul_f32_e32 v18, v18, v18
	v_mul_f32_e32 v19, v19, v19
	v_mul_f32_e32 v20, v8, v16
	v_mul_f32_e32 v24, v9, v16
	v_mul_f32_e32 v21, v8, v17
	v_mul_f32_e32 v25, v9, v17
	v_mul_f32_e32 v22, v8, v18
	v_mul_f32_e32 v26, v9, v18
	v_mul_f32_e32 v23, v8, v19
	v_mul_f32_e32 v27, v9, v19
	v_exp_f32_e32 v20, v20
	v_exp_f32_e32 v21, v21
	v_exp_f32_e32 v22, v22
	v_exp_f32_e32 v23, v23
	v_exp_f32_e32 v24, v24
	v_exp_f32_e32 v25, v25
	v_exp_f32_e32 v26, v26
	v_exp_f32_e32 v27, v27
	v_cvt_pk_f16_f32 v42, v20, v21
	v_cvt_pk_f16_f32 v43, v22, v23
	v_cvt_pk_f16_f32 v74, v24, v25
	v_cvt_pk_f16_f32 v75, v26, v27
	v_add_f32_e32 v16, 0x42c00000, v12
	v_add_f32_e32 v17, 0x42c20000, v12
	v_add_f32_e32 v18, 0x42c40000, v12
	v_add_f32_e32 v19, 0x42c60000, v12
	v_mul_f32_e32 v16, v16, v16
	v_mul_f32_e32 v17, v17, v17
	v_mul_f32_e32 v18, v18, v18
	v_mul_f32_e32 v19, v19, v19
	v_mul_f32_e32 v20, v8, v16
	v_mul_f32_e32 v24, v9, v16
	v_mul_f32_e32 v21, v8, v17
	v_mul_f32_e32 v25, v9, v17
	v_mul_f32_e32 v22, v8, v18
	v_mul_f32_e32 v26, v9, v18
	v_mul_f32_e32 v23, v8, v19
	v_mul_f32_e32 v27, v9, v19
	v_exp_f32_e32 v20, v20
	v_exp_f32_e32 v21, v21
	v_exp_f32_e32 v22, v22
	v_exp_f32_e32 v23, v23
	v_exp_f32_e32 v24, v24
	v_exp_f32_e32 v25, v25
	v_exp_f32_e32 v26, v26
	v_exp_f32_e32 v27, v27
	v_cvt_pk_f16_f32 v44, v20, v21
	v_cvt_pk_f16_f32 v45, v22, v23
	v_cvt_pk_f16_f32 v76, v24, v25
	v_cvt_pk_f16_f32 v77, v26, v27
	v_add_f32_e32 v16, 0x42c80000, v12
	v_add_f32_e32 v17, 0x42ca0000, v12
	v_add_f32_e32 v18, 0x42cc0000, v12
	v_add_f32_e32 v19, 0x42ce0000, v12
	v_mul_f32_e32 v16, v16, v16
	v_mul_f32_e32 v17, v17, v17
	v_mul_f32_e32 v18, v18, v18
	v_mul_f32_e32 v19, v19, v19
	v_mul_f32_e32 v20, v8, v16
	v_mul_f32_e32 v24, v9, v16
	v_mul_f32_e32 v21, v8, v17
	v_mul_f32_e32 v25, v9, v17
	v_mul_f32_e32 v22, v8, v18
	v_mul_f32_e32 v26, v9, v18
	v_mul_f32_e32 v23, v8, v19
	v_mul_f32_e32 v27, v9, v19
	v_exp_f32_e32 v20, v20
	v_exp_f32_e32 v21, v21
	v_exp_f32_e32 v22, v22
	v_exp_f32_e32 v23, v23
	v_exp_f32_e32 v24, v24
	v_exp_f32_e32 v25, v25
	v_exp_f32_e32 v26, v26
	v_exp_f32_e32 v27, v27
	v_cvt_pk_f16_f32 v46, v20, v21
	v_cvt_pk_f16_f32 v47, v22, v23
	v_cvt_pk_f16_f32 v78, v24, v25
	v_cvt_pk_f16_f32 v79, v26, v27
	v_add_u32_e32 v6, 0x8000, v6
	global_load_dwordx4 v[176:179], v6, s[12:13] offset:0 nt
	global_load_dwordx4 v[180:183], v6, s[12:13] offset:1024 nt
	global_load_dwordx4 v[184:187], v6, s[12:13] offset:2048 nt
	global_load_dwordx4 v[188:191], v6, s[12:13] offset:3072 nt
	v_mul_f32_e32 v16, v2, v2
	v_add_f32_e32 v17, 0x3f800000, v2
	v_add_f32_e32 v18, 0x40000000, v2
	v_add_f32_e32 v19, 0x40400000, v2
	v_mul_f32_e32 v17, v17, v17
	v_mul_f32_e32 v18, v18, v18
	v_mul_f32_e32 v19, v19, v19
	v_mul_f32_e32 v20, v28, v16
	v_mul_f32_e32 v24, v29, v16
	v_mul_f32_e32 v21, v28, v17
	v_mul_f32_e32 v25, v29, v17
	v_mul_f32_e32 v22, v28, v18
	v_mul_f32_e32 v26, v29, v18
	v_mul_f32_e32 v23, v28, v19
	v_mul_f32_e32 v27, v29, v19
	v_exp_f32_e32 v20, v20
	v_exp_f32_e32 v21, v21
	v_exp_f32_e32 v22, v22
	v_exp_f32_e32 v23, v23
	v_exp_f32_e32 v24, v24
	v_exp_f32_e32 v25, v25
	v_exp_f32_e32 v26, v26
	v_exp_f32_e32 v27, v27
	v_cvt_pk_f16_f32 v48, v20, v21
	v_cvt_pk_f16_f32 v49, v22, v23
	v_cvt_pk_f16_f32 v80, v24, v25
	v_cvt_pk_f16_f32 v81, v26, v27
	v_add_f32_e32 v16, 0x40800000, v2
	v_add_f32_e32 v17, 0x40a00000, v2
	v_add_f32_e32 v18, 0x40c00000, v2
	v_add_f32_e32 v19, 0x40e00000, v2
	v_mul_f32_e32 v16, v16, v16
	v_mul_f32_e32 v17, v17, v17
	v_mul_f32_e32 v18, v18, v18
	v_mul_f32_e32 v19, v19, v19
	v_mul_f32_e32 v20, v28, v16
	v_mul_f32_e32 v24, v29, v16
	v_mul_f32_e32 v21, v28, v17
	v_mul_f32_e32 v25, v29, v17
	v_mul_f32_e32 v22, v28, v18
	v_mul_f32_e32 v26, v29, v18
	v_mul_f32_e32 v23, v28, v19
	v_mul_f32_e32 v27, v29, v19
	v_exp_f32_e32 v20, v20
	v_exp_f32_e32 v21, v21
	v_exp_f32_e32 v22, v22
	v_exp_f32_e32 v23, v23
	v_exp_f32_e32 v24, v24
	v_exp_f32_e32 v25, v25
	v_exp_f32_e32 v26, v26
	v_exp_f32_e32 v27, v27
	v_cvt_pk_f16_f32 v50, v20, v21
	v_cvt_pk_f16_f32 v51, v22, v23
	v_cvt_pk_f16_f32 v82, v24, v25
	v_cvt_pk_f16_f32 v83, v26, v27
	v_add_f32_e32 v16, 0x42000000, v2
	v_add_f32_e32 v17, 0x42040000, v2
	v_add_f32_e32 v18, 0x42080000, v2
	v_add_f32_e32 v19, 0x420c0000, v2
	v_mul_f32_e32 v16, v16, v16
	v_mul_f32_e32 v17, v17, v17
	v_mul_f32_e32 v18, v18, v18
	v_mul_f32_e32 v19, v19, v19
	v_mul_f32_e32 v20, v28, v16
	v_mul_f32_e32 v24, v29, v16
	v_mul_f32_e32 v21, v28, v17
	v_mul_f32_e32 v25, v29, v17
	v_mul_f32_e32 v22, v28, v18
	v_mul_f32_e32 v26, v29, v18
	v_mul_f32_e32 v23, v28, v19
	v_mul_f32_e32 v27, v29, v19
	v_exp_f32_e32 v20, v20
	v_exp_f32_e32 v21, v21
	v_exp_f32_e32 v22, v22
	v_exp_f32_e32 v23, v23
	v_exp_f32_e32 v24, v24
	v_exp_f32_e32 v25, v25
	v_exp_f32_e32 v26, v26
	v_exp_f32_e32 v27, v27
	v_cvt_pk_f16_f32 v52, v20, v21
	v_cvt_pk_f16_f32 v53, v22, v23
	v_cvt_pk_f16_f32 v84, v24, v25
	v_cvt_pk_f16_f32 v85, v26, v27
	v_add_f32_e32 v16, 0x42100000, v2
	v_add_f32_e32 v17, 0x42140000, v2
	v_add_f32_e32 v18, 0x42180000, v2
	v_add_f32_e32 v19, 0x421c0000, v2
	v_mul_f32_e32 v16, v16, v16
	v_mul_f32_e32 v17, v17, v17
	v_mul_f32_e32 v18, v18, v18
	v_mul_f32_e32 v19, v19, v19
	v_mul_f32_e32 v20, v28, v16
	v_mul_f32_e32 v24, v29, v16
	v_mul_f32_e32 v21, v28, v17
	v_mul_f32_e32 v25, v29, v17
	v_mul_f32_e32 v22, v28, v18
	v_mul_f32_e32 v26, v29, v18
	v_mul_f32_e32 v23, v28, v19
	v_mul_f32_e32 v27, v29, v19
	v_exp_f32_e32 v20, v20
	v_exp_f32_e32 v21, v21
	v_exp_f32_e32 v22, v22
	v_exp_f32_e32 v23, v23
	v_exp_f32_e32 v24, v24
	v_exp_f32_e32 v25, v25
	v_exp_f32_e32 v26, v26
	v_exp_f32_e32 v27, v27
	v_cvt_pk_f16_f32 v54, v20, v21
	v_cvt_pk_f16_f32 v55, v22, v23
	v_cvt_pk_f16_f32 v86, v24, v25
	v_cvt_pk_f16_f32 v87, v26, v27
	v_add_u32_e32 v6, 0x8000, v6
	global_load_dwordx4 v[192:195], v6, s[12:13] offset:0 nt
	global_load_dwordx4 v[196:199], v6, s[12:13] offset:1024 nt
	global_load_dwordx4 v[200:203], v6, s[12:13] offset:2048 nt
	global_load_dwordx4 v[204:207], v6, s[12:13] offset:3072 nt
	v_add_f32_e32 v16, 0x42800000, v2
	v_add_f32_e32 v17, 0x42820000, v2
	v_add_f32_e32 v18, 0x42840000, v2
	v_add_f32_e32 v19, 0x42860000, v2
	v_mul_f32_e32 v16, v16, v16
	v_mul_f32_e32 v17, v17, v17
	v_mul_f32_e32 v18, v18, v18
	v_mul_f32_e32 v19, v19, v19
	v_mul_f32_e32 v20, v28, v16
	v_mul_f32_e32 v24, v29, v16
	v_mul_f32_e32 v21, v28, v17
	v_mul_f32_e32 v25, v29, v17
	v_mul_f32_e32 v22, v28, v18
	v_mul_f32_e32 v26, v29, v18
	v_mul_f32_e32 v23, v28, v19
	v_mul_f32_e32 v27, v29, v19
	v_exp_f32_e32 v20, v20
	v_exp_f32_e32 v21, v21
	v_exp_f32_e32 v22, v22
	v_exp_f32_e32 v23, v23
	v_exp_f32_e32 v24, v24
	v_exp_f32_e32 v25, v25
	v_exp_f32_e32 v26, v26
	v_exp_f32_e32 v27, v27
	v_cvt_pk_f16_f32 v56, v20, v21
	v_cvt_pk_f16_f32 v57, v22, v23
	v_cvt_pk_f16_f32 v88, v24, v25
	v_cvt_pk_f16_f32 v89, v26, v27
	v_add_f32_e32 v16, 0x42880000, v2
	v_add_f32_e32 v17, 0x428a0000, v2
	v_add_f32_e32 v18, 0x428c0000, v2
	v_add_f32_e32 v19, 0x428e0000, v2
	v_mul_f32_e32 v16, v16, v16
	v_mul_f32_e32 v17, v17, v17
	v_mul_f32_e32 v18, v18, v18
	v_mul_f32_e32 v19, v19, v19
	v_mul_f32_e32 v20, v28, v16
	v_mul_f32_e32 v24, v29, v16
	v_mul_f32_e32 v21, v28, v17
	v_mul_f32_e32 v25, v29, v17
	v_mul_f32_e32 v22, v28, v18
	v_mul_f32_e32 v26, v29, v18
	v_mul_f32_e32 v23, v28, v19
	v_mul_f32_e32 v27, v29, v19
	v_exp_f32_e32 v20, v20
	v_exp_f32_e32 v21, v21
	v_exp_f32_e32 v22, v22
	v_exp_f32_e32 v23, v23
	v_exp_f32_e32 v24, v24
	v_exp_f32_e32 v25, v25
	v_exp_f32_e32 v26, v26
	v_exp_f32_e32 v27, v27
	v_cvt_pk_f16_f32 v58, v20, v21
	v_cvt_pk_f16_f32 v59, v22, v23
	v_cvt_pk_f16_f32 v90, v24, v25
	v_cvt_pk_f16_f32 v91, v26, v27
	v_add_f32_e32 v16, 0x42c00000, v2
	v_add_f32_e32 v17, 0x42c20000, v2
	v_add_f32_e32 v18, 0x42c40000, v2
	v_add_f32_e32 v19, 0x42c60000, v2
	v_mul_f32_e32 v16, v16, v16
	v_mul_f32_e32 v17, v17, v17
	v_mul_f32_e32 v18, v18, v18
	v_mul_f32_e32 v19, v19, v19
	v_mul_f32_e32 v20, v28, v16
	v_mul_f32_e32 v24, v29, v16
	v_mul_f32_e32 v21, v28, v17
	v_mul_f32_e32 v25, v29, v17
	v_mul_f32_e32 v22, v28, v18
	v_mul_f32_e32 v26, v29, v18
	v_mul_f32_e32 v23, v28, v19
	v_mul_f32_e32 v27, v29, v19
	v_exp_f32_e32 v20, v20
	v_exp_f32_e32 v21, v21
	v_exp_f32_e32 v22, v22
	v_exp_f32_e32 v23, v23
	v_exp_f32_e32 v24, v24
	v_exp_f32_e32 v25, v25
	v_exp_f32_e32 v26, v26
	v_exp_f32_e32 v27, v27
	v_cvt_pk_f16_f32 v60, v20, v21
	v_cvt_pk_f16_f32 v61, v22, v23
	v_cvt_pk_f16_f32 v92, v24, v25
	v_cvt_pk_f16_f32 v93, v26, v27
	v_add_f32_e32 v16, 0x42c80000, v2
	v_add_f32_e32 v17, 0x42ca0000, v2
	v_add_f32_e32 v18, 0x42cc0000, v2
	v_add_f32_e32 v19, 0x42ce0000, v2
	v_mul_f32_e32 v16, v16, v16
	v_mul_f32_e32 v17, v17, v17
	v_mul_f32_e32 v18, v18, v18
	v_mul_f32_e32 v19, v19, v19
	v_mul_f32_e32 v20, v28, v16
	v_mul_f32_e32 v24, v29, v16
	v_mul_f32_e32 v21, v28, v17
	v_mul_f32_e32 v25, v29, v17
	v_mul_f32_e32 v22, v28, v18
	v_mul_f32_e32 v26, v29, v18
	v_mul_f32_e32 v23, v28, v19
	v_mul_f32_e32 v27, v29, v19
	v_exp_f32_e32 v20, v20
	v_exp_f32_e32 v21, v21
	v_exp_f32_e32 v22, v22
	v_exp_f32_e32 v23, v23
	v_exp_f32_e32 v24, v24
	v_exp_f32_e32 v25, v25
	v_exp_f32_e32 v26, v26
	v_exp_f32_e32 v27, v27
	v_cvt_pk_f16_f32 v62, v20, v21
	v_cvt_pk_f16_f32 v63, v22, v23
	v_cvt_pk_f16_f32 v94, v24, v25
	v_cvt_pk_f16_f32 v95, v26, v27
	v_add_u32_e32 v6, 0x8000, v6
	global_load_dwordx4 v[208:211], v6, s[12:13] offset:0 nt
	global_load_dwordx4 v[212:215], v6, s[12:13] offset:1024 nt
	global_load_dwordx4 v[216:219], v6, s[12:13] offset:2048 nt
	global_load_dwordx4 v[220:223], v6, s[12:13] offset:3072 nt
	v_mul_f32_e32 v16, v13, v13
	v_add_f32_e32 v17, 0x3f800000, v13
	v_add_f32_e32 v18, 0x40000000, v13
	v_add_f32_e32 v19, 0x40400000, v13
	v_mul_f32_e32 v17, v17, v17
	v_mul_f32_e32 v18, v18, v18
	v_mul_f32_e32 v19, v19, v19
	v_mul_f32_e32 v20, v8, v16
	v_mul_f32_e32 v24, v9, v16
	v_mul_f32_e32 v21, v8, v17
	v_mul_f32_e32 v25, v9, v17
	v_mul_f32_e32 v22, v8, v18
	v_mul_f32_e32 v26, v9, v18
	v_mul_f32_e32 v23, v8, v19
	v_mul_f32_e32 v27, v9, v19
	v_exp_f32_e32 v20, v20
	v_exp_f32_e32 v21, v21
	v_exp_f32_e32 v22, v22
	v_exp_f32_e32 v23, v23
	v_exp_f32_e32 v24, v24
	v_exp_f32_e32 v25, v25
	v_exp_f32_e32 v26, v26
	v_exp_f32_e32 v27, v27
	v_mul_f32_e32 v96, v10, v20
	v_mul_f32_e32 v97, v10, v21
	v_mul_f32_e32 v98, v10, v22
	v_mul_f32_e32 v99, v10, v23
	v_mul_f32_e32 v112, v11, v24
	v_mul_f32_e32 v113, v11, v25
	v_mul_f32_e32 v114, v11, v26
	v_mul_f32_e32 v115, v11, v27
	v_add_f32_e32 v16, 0x41800000, v13
	v_add_f32_e32 v17, 0x41880000, v13
	v_add_f32_e32 v18, 0x41900000, v13
	v_add_f32_e32 v19, 0x41980000, v13
	v_mul_f32_e32 v16, v16, v16
	v_mul_f32_e32 v17, v17, v17
	v_mul_f32_e32 v18, v18, v18
	v_mul_f32_e32 v19, v19, v19
	v_mul_f32_e32 v20, v8, v16
	v_mul_f32_e32 v24, v9, v16
	v_mul_f32_e32 v21, v8, v17
	v_mul_f32_e32 v25, v9, v17
	v_mul_f32_e32 v22, v8, v18
	v_mul_f32_e32 v26, v9, v18
	v_mul_f32_e32 v23, v8, v19
	v_mul_f32_e32 v27, v9, v19
	v_exp_f32_e32 v20, v20
	v_exp_f32_e32 v21, v21
	v_exp_f32_e32 v22, v22
	v_exp_f32_e32 v23, v23
	v_exp_f32_e32 v24, v24
	v_exp_f32_e32 v25, v25
	v_exp_f32_e32 v26, v26
	v_exp_f32_e32 v27, v27
	v_mul_f32_e32 v100, v10, v20
	v_mul_f32_e32 v101, v10, v21
	v_mul_f32_e32 v102, v10, v22
	v_mul_f32_e32 v103, v10, v23
	v_mul_f32_e32 v116, v11, v24
	v_mul_f32_e32 v117, v11, v25
	v_mul_f32_e32 v118, v11, v26
	v_mul_f32_e32 v119, v11, v27
	v_add_u32_e32 v6, 0x8000, v6
	global_load_dwordx4 v[224:227], v6, s[12:13] offset:0 nt
	global_load_dwordx4 v[228:231], v6, s[12:13] offset:1024 nt
	global_load_dwordx4 v[232:235], v6, s[12:13] offset:2048 nt
	global_load_dwordx4 v[236:239], v6, s[12:13] offset:3072 nt
	v_mul_f32_e32 v16, v3, v3
	v_add_f32_e32 v17, 0x3f800000, v3
	v_add_f32_e32 v18, 0x40000000, v3
	v_add_f32_e32 v19, 0x40400000, v3
	v_mul_f32_e32 v17, v17, v17
	v_mul_f32_e32 v18, v18, v18
	v_mul_f32_e32 v19, v19, v19
	v_mul_f32_e32 v20, v28, v16
	v_mul_f32_e32 v24, v29, v16
	v_mul_f32_e32 v21, v28, v17
	v_mul_f32_e32 v25, v29, v17
	v_mul_f32_e32 v22, v28, v18
	v_mul_f32_e32 v26, v29, v18
	v_mul_f32_e32 v23, v28, v19
	v_mul_f32_e32 v27, v29, v19
	v_exp_f32_e32 v20, v20
	v_exp_f32_e32 v21, v21
	v_exp_f32_e32 v22, v22
	v_exp_f32_e32 v23, v23
	v_exp_f32_e32 v24, v24
	v_exp_f32_e32 v25, v25
	v_exp_f32_e32 v26, v26
	v_exp_f32_e32 v27, v27
	v_mul_f32_e32 v104, v30, v20
	v_mul_f32_e32 v105, v30, v21
	v_mul_f32_e32 v106, v30, v22
	v_mul_f32_e32 v107, v30, v23
	v_mul_f32_e32 v120, v31, v24
	v_mul_f32_e32 v121, v31, v25
	v_mul_f32_e32 v122, v31, v26
	v_mul_f32_e32 v123, v31, v27
	v_add_f32_e32 v16, 0x41800000, v3
	v_add_f32_e32 v17, 0x41880000, v3
	v_add_f32_e32 v18, 0x41900000, v3
	v_add_f32_e32 v19, 0x41980000, v3
	v_mul_f32_e32 v16, v16, v16
	v_mul_f32_e32 v17, v17, v17
	v_mul_f32_e32 v18, v18, v18
	v_mul_f32_e32 v19, v19, v19
	v_mul_f32_e32 v20, v28, v16
	v_mul_f32_e32 v24, v29, v16
	v_mul_f32_e32 v21, v28, v17
	v_mul_f32_e32 v25, v29, v17
	v_mul_f32_e32 v22, v28, v18
	v_mul_f32_e32 v26, v29, v18
	v_mul_f32_e32 v23, v28, v19
	v_mul_f32_e32 v27, v29, v19
	v_exp_f32_e32 v20, v20
	v_exp_f32_e32 v21, v21
	v_exp_f32_e32 v22, v22
	v_exp_f32_e32 v23, v23
	v_exp_f32_e32 v24, v24
	v_exp_f32_e32 v25, v25
	v_exp_f32_e32 v26, v26
	v_exp_f32_e32 v27, v27
	v_mul_f32_e32 v108, v30, v20
	v_mul_f32_e32 v109, v30, v21
	v_mul_f32_e32 v110, v30, v22
	v_mul_f32_e32 v111, v30, v23
	v_mul_f32_e32 v124, v31, v24
	v_mul_f32_e32 v125, v31, v25
	v_mul_f32_e32 v126, v31, v26
	v_mul_f32_e32 v127, v31, v27
	v_add_u32_e32 v6, 0x8000, v6
	global_load_dwordx4 v[240:243], v6, s[12:13] offset:0 nt
	global_load_dwordx4 v[244:247], v6, s[12:13] offset:1024 nt
	global_load_dwordx4 v[248:251], v6, s[12:13] offset:2048 nt
	global_load_dwordx4 v[252:255], v6, s[12:13] offset:3072 nt
	s_waitcnt vmcnt(28)
	v_add_f32_e32 v128, v128, v129
	v_add_f32_e32 v130, v130, v131
	v_add_f32_e32 v132, v132, v133
	v_add_f32_e32 v134, v134, v135
	v_add_f32_e32 v136, v136, v137
	v_add_f32_e32 v138, v138, v139
	v_add_f32_e32 v140, v140, v141
	v_add_f32_e32 v142, v142, v143
	v_add_f32_e32 v128, v128, v130
	v_add_f32_e32 v132, v132, v134
	v_add_f32_e32 v136, v136, v138
	v_add_f32_e32 v140, v140, v142
	v_cndmask_b32_e64 v130, v128, v132, s[30:31]
	v_cndmask_b32_e64 v134, v136, v140, s[30:31]
	v_cndmask_b32_e64 v129, v132, v128, s[30:31]
	v_cndmask_b32_e64 v133, v140, v136, s[30:31]
	v_add_f32_dpp v129, v130, v129 quad_perm:[1,0,3,2] row_mask:0xf bank_mask:0xf bound_ctrl:1
	v_add_f32_dpp v133, v134, v133 quad_perm:[1,0,3,2] row_mask:0xf bank_mask:0xf bound_ctrl:1
	v_cndmask_b32_e64 v135, v129, v133, s[32:33]
	v_cndmask_b32_e64 v131, v133, v129, s[32:33]
	s_nop 1
	v_add_f32_dpp v131, v135, v131 quad_perm:[2,3,0,1] row_mask:0xf bank_mask:0xf bound_ctrl:1
	v_cvt_f16_f32_e32 v131, v131
	ds_write_b16 v14, v131 offset:0
	s_waitcnt vmcnt(24)
	v_add_f32_e32 v144, v144, v145
	v_add_f32_e32 v146, v146, v147
	v_add_f32_e32 v148, v148, v149
	v_add_f32_e32 v150, v150, v151
	v_add_f32_e32 v152, v152, v153
	v_add_f32_e32 v154, v154, v155
	v_add_f32_e32 v156, v156, v157
	v_add_f32_e32 v158, v158, v159
	v_add_f32_e32 v144, v144, v146
	v_add_f32_e32 v148, v148, v150
	v_add_f32_e32 v152, v152, v154
	v_add_f32_e32 v156, v156, v158
	v_cndmask_b32_e64 v146, v144, v148, s[30:31]
	v_cndmask_b32_e64 v150, v152, v156, s[30:31]
	v_cndmask_b32_e64 v145, v148, v144, s[30:31]
	v_cndmask_b32_e64 v149, v156, v152, s[30:31]
	v_add_f32_dpp v145, v146, v145 quad_perm:[1,0,3,2] row_mask:0xf bank_mask:0xf bound_ctrl:1
	v_add_f32_dpp v149, v150, v149 quad_perm:[1,0,3,2] row_mask:0xf bank_mask:0xf bound_ctrl:1
	v_cndmask_b32_e64 v151, v145, v149, s[32:33]
	v_cndmask_b32_e64 v147, v149, v145, s[32:33]
	s_nop 1
	v_add_f32_dpp v147, v151, v147 quad_perm:[2,3,0,1] row_mask:0xf bank_mask:0xf bound_ctrl:1
	v_cvt_f16_f32_e32 v147, v147
	ds_write_b16 v14, v147 offset:1088
	s_waitcnt vmcnt(20)
	v_add_f32_e32 v160, v160, v161
	v_add_f32_e32 v162, v162, v163
	v_add_f32_e32 v164, v164, v165
	v_add_f32_e32 v166, v166, v167
	v_add_f32_e32 v168, v168, v169
	v_add_f32_e32 v170, v170, v171
	v_add_f32_e32 v172, v172, v173
	v_add_f32_e32 v174, v174, v175
	v_add_f32_e32 v160, v160, v162
	v_add_f32_e32 v164, v164, v166
	v_add_f32_e32 v168, v168, v170
	v_add_f32_e32 v172, v172, v174
	v_cndmask_b32_e64 v162, v160, v164, s[30:31]
	v_cndmask_b32_e64 v166, v168, v172, s[30:31]
	v_cndmask_b32_e64 v161, v164, v160, s[30:31]
	v_cndmask_b32_e64 v165, v172, v168, s[30:31]
	v_add_f32_dpp v161, v162, v161 quad_perm:[1,0,3,2] row_mask:0xf bank_mask:0xf bound_ctrl:1
	v_add_f32_dpp v165, v166, v165 quad_perm:[1,0,3,2] row_mask:0xf bank_mask:0xf bound_ctrl:1
	v_cndmask_b32_e64 v167, v161, v165, s[32:33]
	v_cndmask_b32_e64 v163, v165, v161, s[32:33]
	s_nop 1
	v_add_f32_dpp v163, v167, v163 quad_perm:[2,3,0,1] row_mask:0xf bank_mask:0xf bound_ctrl:1
	v_cvt_f16_f32_e32 v163, v163
	ds_write_b16 v14, v163 offset:2176
	s_waitcnt vmcnt(16)
	v_add_f32_e32 v176, v176, v177
	v_add_f32_e32 v178, v178, v179
	v_add_f32_e32 v180, v180, v181
	v_add_f32_e32 v182, v182, v183
	v_add_f32_e32 v184, v184, v185
	v_add_f32_e32 v186, v186, v187
	v_add_f32_e32 v188, v188, v189
	v_add_f32_e32 v190, v190, v191
	v_add_f32_e32 v176, v176, v178
	v_add_f32_e32 v180, v180, v182
	v_add_f32_e32 v184, v184, v186
	v_add_f32_e32 v188, v188, v190
	v_cndmask_b32_e64 v178, v176, v180, s[30:31]
	v_cndmask_b32_e64 v182, v184, v188, s[30:31]
	v_cndmask_b32_e64 v177, v180, v176, s[30:31]
	v_cndmask_b32_e64 v181, v188, v184, s[30:31]
	v_add_f32_dpp v177, v178, v177 quad_perm:[1,0,3,2] row_mask:0xf bank_mask:0xf bound_ctrl:1
	v_add_f32_dpp v181, v182, v181 quad_perm:[1,0,3,2] row_mask:0xf bank_mask:0xf bound_ctrl:1
	v_cndmask_b32_e64 v183, v177, v181, s[32:33]
	v_cndmask_b32_e64 v179, v181, v177, s[32:33]
	s_nop 1
	v_add_f32_dpp v179, v183, v179 quad_perm:[2,3,0,1] row_mask:0xf bank_mask:0xf bound_ctrl:1
	v_cvt_f16_f32_e32 v179, v179
	ds_write_b16 v14, v179 offset:3264
	s_waitcnt lgkmcnt(0)
	s_barrier
	ds_read_b128 v[160:163], v15 offset:0
	ds_read_b128 v[164:167], v15 offset:64
	ds_read_b128 v[168:171], v15 offset:128
	ds_read_b128 v[172:175], v15 offset:192
	s_waitcnt lgkmcnt(3)
	v_mfma_f32_16x16x32_f16 v[128:131], v[160:163], v[32:35], 0
	v_mfma_f32_16x16x32_f16 v[144:147], v[160:163], v[64:67], 0
	v_mfma_f32_16x16x32_f16 v[136:139], v[160:163], v[48:51], 0
	v_mfma_f32_16x16x32_f16 v[152:155], v[160:163], v[80:83], 0
	s_waitcnt lgkmcnt(2)
	v_mfma_f32_16x16x32_f16 v[128:131], v[164:167], v[36:39], v[128:131]
	v_mfma_f32_16x16x32_f16 v[144:147], v[164:167], v[68:71], v[144:147]
	v_mfma_f32_16x16x32_f16 v[136:139], v[164:167], v[52:55], v[136:139]
	v_mfma_f32_16x16x32_f16 v[152:155], v[164:167], v[84:87], v[152:155]
	s_waitcnt lgkmcnt(1)
	v_mfma_f32_16x16x32_f16 v[128:131], v[168:171], v[40:43], v[128:131]
	v_mfma_f32_16x16x32_f16 v[144:147], v[168:171], v[72:75], v[144:147]
	v_mfma_f32_16x16x32_f16 v[136:139], v[168:171], v[56:59], v[136:139]
	v_mfma_f32_16x16x32_f16 v[152:155], v[168:171], v[88:91], v[152:155]
	s_waitcnt lgkmcnt(0)
	v_mfma_f32_16x16x32_f16 v[128:131], v[172:175], v[44:47], v[128:131]
	v_mfma_f32_16x16x32_f16 v[144:147], v[172:175], v[76:79], v[144:147]
	v_mfma_f32_16x16x32_f16 v[136:139], v[172:175], v[60:63], v[136:139]
	v_mfma_f32_16x16x32_f16 v[152:155], v[172:175], v[92:95], v[152:155]
	s_waitcnt vmcnt(12)
	v_add_f32_e32 v192, v192, v193
	v_add_f32_e32 v194, v194, v195
	v_add_f32_e32 v196, v196, v197
	v_add_f32_e32 v198, v198, v199
	v_add_f32_e32 v200, v200, v201
	v_add_f32_e32 v202, v202, v203
	v_add_f32_e32 v204, v204, v205
	v_add_f32_e32 v206, v206, v207
	v_add_f32_e32 v192, v192, v194
	v_add_f32_e32 v196, v196, v198
	v_add_f32_e32 v200, v200, v202
	v_add_f32_e32 v204, v204, v206
	v_cndmask_b32_e64 v194, v192, v196, s[30:31]
	v_cndmask_b32_e64 v198, v200, v204, s[30:31]
	v_cndmask_b32_e64 v193, v196, v192, s[30:31]
	v_cndmask_b32_e64 v197, v204, v200, s[30:31]
	v_add_f32_dpp v193, v194, v193 quad_perm:[1,0,3,2] row_mask:0xf bank_mask:0xf bound_ctrl:1
	v_add_f32_dpp v197, v198, v197 quad_perm:[1,0,3,2] row_mask:0xf bank_mask:0xf bound_ctrl:1
	v_cndmask_b32_e64 v199, v193, v197, s[32:33]
	v_cndmask_b32_e64 v195, v197, v193, s[32:33]
	s_nop 1
	v_add_f32_dpp v195, v199, v195 quad_perm:[2,3,0,1] row_mask:0xf bank_mask:0xf bound_ctrl:1
	v_cvt_f16_f32_e32 v195, v195
	ds_write_b16 v14, v195 offset:4352
	s_waitcnt vmcnt(8)
	v_add_f32_e32 v208, v208, v209
	v_add_f32_e32 v210, v210, v211
	v_add_f32_e32 v212, v212, v213
	v_add_f32_e32 v214, v214, v215
	v_add_f32_e32 v216, v216, v217
	v_add_f32_e32 v218, v218, v219
	v_add_f32_e32 v220, v220, v221
	v_add_f32_e32 v222, v222, v223
	v_add_f32_e32 v208, v208, v210
	v_add_f32_e32 v212, v212, v214
	v_add_f32_e32 v216, v216, v218
	v_add_f32_e32 v220, v220, v222
	v_cndmask_b32_e64 v210, v208, v212, s[30:31]
	v_cndmask_b32_e64 v214, v216, v220, s[30:31]
	v_cndmask_b32_e64 v209, v212, v208, s[30:31]
	v_cndmask_b32_e64 v213, v220, v216, s[30:31]
	v_add_f32_dpp v209, v210, v209 quad_perm:[1,0,3,2] row_mask:0xf bank_mask:0xf bound_ctrl:1
	v_add_f32_dpp v213, v214, v213 quad_perm:[1,0,3,2] row_mask:0xf bank_mask:0xf bound_ctrl:1
	v_cndmask_b32_e64 v215, v209, v213, s[32:33]
	v_cndmask_b32_e64 v211, v213, v209, s[32:33]
	s_nop 1
	v_add_f32_dpp v211, v215, v211 quad_perm:[2,3,0,1] row_mask:0xf bank_mask:0xf bound_ctrl:1
	v_cvt_f16_f32_e32 v211, v211
	ds_write_b16 v14, v211 offset:5440
	s_waitcnt vmcnt(4)
	v_add_f32_e32 v224, v224, v225
	v_add_f32_e32 v226, v226, v227
	v_add_f32_e32 v228, v228, v229
	v_add_f32_e32 v230, v230, v231
	v_add_f32_e32 v232, v232, v233
	v_add_f32_e32 v234, v234, v235
	v_add_f32_e32 v236, v236, v237
	v_add_f32_e32 v238, v238, v239
	v_add_f32_e32 v224, v224, v226
	v_add_f32_e32 v228, v228, v230
	v_add_f32_e32 v232, v232, v234
	v_add_f32_e32 v236, v236, v238
	v_cndmask_b32_e64 v226, v224, v228, s[30:31]
	v_cndmask_b32_e64 v230, v232, v236, s[30:31]
	v_cndmask_b32_e64 v225, v228, v224, s[30:31]
	v_cndmask_b32_e64 v229, v236, v232, s[30:31]
	v_add_f32_dpp v225, v226, v225 quad_perm:[1,0,3,2] row_mask:0xf bank_mask:0xf bound_ctrl:1
	v_add_f32_dpp v229, v230, v229 quad_perm:[1,0,3,2] row_mask:0xf bank_mask:0xf bound_ctrl:1
	v_cndmask_b32_e64 v231, v225, v229, s[32:33]
	v_cndmask_b32_e64 v227, v229, v225, s[32:33]
	s_nop 1
	v_add_f32_dpp v227, v231, v227 quad_perm:[2,3,0,1] row_mask:0xf bank_mask:0xf bound_ctrl:1
	v_cvt_f16_f32_e32 v227, v227
	ds_write_b16 v14, v227 offset:6528
	s_waitcnt vmcnt(0)
	v_add_f32_e32 v240, v240, v241
	v_add_f32_e32 v242, v242, v243
	v_add_f32_e32 v244, v244, v245
	v_add_f32_e32 v246, v246, v247
	v_add_f32_e32 v248, v248, v249
	v_add_f32_e32 v250, v250, v251
	v_add_f32_e32 v252, v252, v253
	v_add_f32_e32 v254, v254, v255
	v_add_f32_e32 v240, v240, v242
	v_add_f32_e32 v244, v244, v246
	v_add_f32_e32 v248, v248, v250
	v_add_f32_e32 v252, v252, v254
	v_cndmask_b32_e64 v242, v240, v244, s[30:31]
	v_cndmask_b32_e64 v246, v248, v252, s[30:31]
	v_cndmask_b32_e64 v241, v244, v240, s[30:31]
	v_cndmask_b32_e64 v245, v252, v248, s[30:31]
	v_add_f32_dpp v241, v242, v241 quad_perm:[1,0,3,2] row_mask:0xf bank_mask:0xf bound_ctrl:1
	v_add_f32_dpp v245, v246, v245 quad_perm:[1,0,3,2] row_mask:0xf bank_mask:0xf bound_ctrl:1
	v_cndmask_b32_e64 v247, v241, v245, s[32:33]
	v_cndmask_b32_e64 v243, v245, v241, s[32:33]
	s_nop 1
	v_add_f32_dpp v243, v247, v243 quad_perm:[2,3,0,1] row_mask:0xf bank_mask:0xf bound_ctrl:1
	v_cvt_f16_f32_e32 v243, v243
	ds_write_b16 v14, v243 offset:7616
	s_waitcnt lgkmcnt(0)
	s_barrier
	ds_read_b128 v[160:163], v15 offset:4352
	ds_read_b128 v[164:167], v15 offset:4416
	ds_read_b128 v[168:171], v15 offset:4480
	ds_read_b128 v[172:175], v15 offset:4544
	s_waitcnt lgkmcnt(3)
	v_mfma_f32_16x16x32_f16 v[132:135], v[160:163], v[32:35], 0
	v_mfma_f32_16x16x32_f16 v[148:151], v[160:163], v[64:67], 0
	v_mfma_f32_16x16x32_f16 v[140:143], v[160:163], v[48:51], 0
	v_mfma_f32_16x16x32_f16 v[156:159], v[160:163], v[80:83], 0
	s_waitcnt lgkmcnt(2)
	v_mfma_f32_16x16x32_f16 v[132:135], v[164:167], v[36:39], v[132:135]
	v_mfma_f32_16x16x32_f16 v[148:151], v[164:167], v[68:71], v[148:151]
	v_mfma_f32_16x16x32_f16 v[140:143], v[164:167], v[52:55], v[140:143]
	v_mfma_f32_16x16x32_f16 v[156:159], v[164:167], v[84:87], v[156:159]
	s_waitcnt lgkmcnt(1)
	v_mfma_f32_16x16x32_f16 v[132:135], v[168:171], v[40:43], v[132:135]
	v_mfma_f32_16x16x32_f16 v[148:151], v[168:171], v[72:75], v[148:151]
	v_mfma_f32_16x16x32_f16 v[140:143], v[168:171], v[56:59], v[140:143]
	v_mfma_f32_16x16x32_f16 v[156:159], v[168:171], v[88:91], v[156:159]
	s_waitcnt lgkmcnt(0)
	v_mfma_f32_16x16x32_f16 v[132:135], v[172:175], v[44:47], v[132:135]
	v_mfma_f32_16x16x32_f16 v[148:151], v[172:175], v[76:79], v[148:151]
	v_mfma_f32_16x16x32_f16 v[140:143], v[172:175], v[60:63], v[140:143]
	v_mfma_f32_16x16x32_f16 v[156:159], v[172:175], v[92:95], v[156:159]
	s_nop 15
	v_mul_f32_e32 v16, v96, v128
	v_mul_f32_e32 v17, v100, v132
	v_mul_f32_e32 v18, v104, v136
	v_mul_f32_e32 v19, v108, v140
	v_fma_f32 v16, -v112, v144, v16
	v_fma_f32 v17, -v116, v148, v17
	v_fma_f32 v18, -v120, v152, v18
	v_fma_f32 v19, -v124, v156, v19
	v_fma_f32 v16, v97, v129, v16
	v_fma_f32 v16, -v113, v145, v16
	v_fma_f32 v17, v101, v133, v17
	v_fma_f32 v17, -v117, v149, v17
	v_fma_f32 v18, v105, v137, v18
	v_fma_f32 v18, -v121, v153, v18
	v_fma_f32 v19, v109, v141, v19
	v_fma_f32 v19, -v125, v157, v19
	v_fma_f32 v16, v98, v130, v16
	v_fma_f32 v16, -v114, v146, v16
	v_fma_f32 v17, v102, v134, v17
	v_fma_f32 v17, -v118, v150, v17
	v_fma_f32 v18, v106, v138, v18
	v_fma_f32 v18, -v122, v154, v18
	v_fma_f32 v19, v110, v142, v19
	v_fma_f32 v19, -v126, v158, v19
	v_fma_f32 v16, v99, v131, v16
	v_fma_f32 v16, -v115, v147, v16
	v_fma_f32 v17, v103, v135, v17
	v_fma_f32 v17, -v119, v151, v17
	v_fma_f32 v18, v107, v139, v18
	v_fma_f32 v18, -v123, v155, v18
	v_fma_f32 v19, v111, v143, v19
	v_fma_f32 v19, -v127, v159, v19
	v_add_f32_e32 v16, v16, v17
	v_add_f32_e32 v18, v18, v19
	s_lshl_b32 s6, s6, 6
	s_add_i32 s6, s6, s7
	s_lshl_b32 s6, s6, 10
	v_permlane16_swap_b32_e32 v16, v18
	v_add_u32_e32 v5, s6, v5
	v_add_f32_e32 v16, v16, v18
	v_mov_b32_e32 v17, v16
	v_cmp_gt_u32_e32 vcc, 32, v1
	s_nop 0
	v_permlane32_swap_b32_e32 v16, v17
	s_nop 0
	v_add_f32_e32 v16, v16, v17
	s_and_saveexec_b64 s[2:3], vcc
	s_cbranch_execz .Ldog_main_done
	global_store_dword v5, v16, s[26:27]
